# speedup vs baseline: 1.0683x; 1.0064x over previous
.LBB0_2:
	s_cmp_eq_u32 s36, 7
	s_cbranch_scc0 .Lprod_end
	s_cmp_lt_u32 s2, 8
	s_cbranch_scc0 .Lprod_end
	s_mov_b64 exec, -1
	buffer_wbl2 sc1
